# outwarm
# baseline (speedup 1.0000x reference)
_Z11attn_kernelILi4EEvPKfS1_S1_S1_S1_S1_PKcPf:
	s_load_dwordx2 s[24:25], s[0:1], 0x30
	s_load_dwordx8 s[8:15], s[0:1], 0x0
	s_load_dwordx4 s[16:19], s[0:1], 0x20
	s_load_dwordx2 s[34:35], s[0:1], 0x38
	v_lshrrev_b32_e32 v63, 6, v0
	v_and_b32_e32 v57, 15, v0
	v_bfe_u32 v1, v0, 4, 2
	v_lshrrev_b32_e32 v2, 2, v57
	v_mul_u32_u24_e32 v4, 3, v1
	v_mul_u32_u24_e32 v2, 3, v2
	v_mad_u32_u24 v4, v63, 12, v4
	v_mad_u32_u24 v2, v63, 12, v2
	v_lshlrev_b32_e32 v4, 2, v4
	v_lshlrev_b32_e32 v2, 2, v2
	v_and_b32_e32 v104, 63, v0
	v_lshlrev_b32_e32 v60, 5, v57
	v_lshlrev_b32_e32 v58, 3, v1
	v_add_u32_e32 v3, v60, v58
	v_lshrrev_b32_e32 v56, 4, v0
	v_lshlrev_b32_e32 v54, 4, v57
	v_mov_b32_e32 v59, 0
	s_movk_i32 s4, 0xe0
	v_cmp_gt_u32_e64 s[4:5], s4, v0
	s_lshl_b32 s26, s2, 8
	s_lshl_b32 s27, s2, 9
	s_mul_i32 s28, s2, 14
	s_add_u32 s26, s26, 0x164000
	s_add_u32 s27, s27, 0x80000
	s_add_u32 s20, s26, 0xc0
	v_lshlrev_b32_e32 v5, 2, v57
	v_lshlrev_b32_e32 v147, 6, v57
	v_add_u32_e32 v2, s26, v2
	v_add_u32_e32 v4, s26, v4
	v_add_u32_e32 v3, s27, v3
	v_mul_u32_u24_e32 v156, 0x140, v1
	s_movk_i32 s21, 0x500
	v_mad_u32_u24 v156, v63, s21, v156
	v_lshl_or_b32 v156, v57, 2, v156
	v_add_u32_e32 v156, 0x1c00, v156
	v_lshlrev_b32_e32 v157, 5, v56
	v_cmp_gt_u32_e32 vcc, 3, v57
	v_add_u32_e32 v158, 4, v57
	v_lshlrev_b32_e32 v159, 2, v57
	s_movk_i32 s21, 0x50
	v_cndmask_b32_e32 v158, 4, v158, vcc
	v_mad_u32_u24 v159, v56, s21, v159
	v_lshl_add_u32 v158, v158, 2, v157
	v_mul_u32_u24_e32 v250, 0x50, v56
	v_or_b32_e32 v250, 0x3800, v250
	v_lshl_add_u32 v251, v57, 1, v250
	v_mul_u32_u24_e32 v252, 0x50, v57
	v_lshl_add_u32 v252, v58, 1, v252
	v_lshlrev_b32_e32 v253, 2, v57
	v_and_b32_e32 v254, 0xc0, v0
	v_lshlrev_b32_e32 v255, 11, v1
	v_or3_b32 v253, v253, v254, v255
	v_add_u32_e32 v254, s28, v56
	v_lshl_add_u32 v254, v254, 9, v54
	v_lshl_or_b32 v255, v56, 9, v54
	s_waitcnt lgkmcnt(0)
	global_load_dwordx3 v[80:82], v2, s[24:25]
	global_load_dwordx3 v[84:86], v4, s[24:25]
	global_load_dwordx2 v[64:65], v3, s[24:25]
	s_load_dword s3, s[24:25], s20
	s_add_u32 s22, s24, 0x160000
	s_addc_u32 s23, s25, 0
	v_cndmask_b32_e64 v62, 13, v56, s[4:5]
	v_add_u32_e32 v3, s28, v62
	v_mad_u32_u24 v144, v3, 36, v5
	v_mad_u32_u24 v146, v3, 12, v5
	v_add_u32_e32 v145, -36, v146
	v_add_u32_e32 v146, -48, v146
	v_lshl_or_b32 v147, v63, 10, v147
	v_lshl_or_b32 v147, v1, 4, v147
	v_or_b32_e32 v148, 0x1000, v147
	v_lshlrev_b32_e32 v149, 4, v104
	v_lshlrev_b32_e32 v150, 9, v3
	v_add_u32_e32 v150, v150, v54
	v_and_b32_e32 v87, 3, v57
	v_lshlrev_b32_e32 v87, 4, v87
	v_lshl_or_b32 v87, v1, 6, v87
	v_lshlrev_b32_e32 v88, 3, v57
	s_add_u32 s26, s24, 0x100000
	s_addc_u32 s27, s25, 0
	s_add_u32 s28, s24, 0x140000
	s_addc_u32 s29, s25, 0
	s_movk_i32 s6, 0x140
	v_cmp_gt_u32_e32 vcc, s6, v0
	v_lshlrev_b32_e32 v22, 2, v0
	v_mov_b32_e32 v23, 0
	s_and_saveexec_b64 s[6:7], vcc
	ds_write_b32 v22, v23 offset:14336
	s_or_b64 exec, exec, s[6:7]
	v_cmp_gt_u32_e32 vcc, 64, v0
	s_and_saveexec_b64 s[6:7], vcc
	ds_write_b32 v22, v23 offset:15360
	s_or_b64 exec, exec, s[6:7]
	v_mov_b32_e32 v45, 0xc9c35000
	s_mov_b32 s30, 0x3db8aa3b
	s_mov_b32 s31, 0x3db8aa3b
	v_mov_b32_e32 v121, 0x3fb8aa3b
	v_mov_b32_e32 v35, 0
	v_mov_b32_e32 v44, v45
	s_waitcnt lgkmcnt(0)
	s_bitcmp0_b32 s3, 1
	s_cselect_b64 s[20:21], -1, 0
	s_cbranch_scc1 .LBB1_16
	v_bfe_u32 v46, s3, v57, 1
	v_cmp_eq_u32_e32 vcc, 0, v46
	s_nop 1
	v_cndmask_b32_e32 v47, 0, v45, vcc
	v_cndmask_b32_e64 v55, 1.0, 0, vcc
	s_nop 0
	v_mov_b32_dpp v34, v47 row_newbcast:0 row_mask:0xf bank_mask:0xf bound_ctrl:1
	v_mov_b32_dpp v36, v47 row_newbcast:2 row_mask:0xf bank_mask:0xf bound_ctrl:1
	v_mov_b32_dpp v37, v47 row_newbcast:3 row_mask:0xf bank_mask:0xf bound_ctrl:1
	v_mov_b32_dpp v22, v47 row_newbcast:4 row_mask:0xf bank_mask:0xf bound_ctrl:1
	v_mov_b32_dpp v23, v47 row_newbcast:5 row_mask:0xf bank_mask:0xf bound_ctrl:1
	v_mov_b32_dpp v24, v47 row_newbcast:6 row_mask:0xf bank_mask:0xf bound_ctrl:1
	v_mov_b32_dpp v25, v47 row_newbcast:7 row_mask:0xf bank_mask:0xf bound_ctrl:1
	v_mov_b32_dpp v38, v47 row_newbcast:8 row_mask:0xf bank_mask:0xf bound_ctrl:1
	v_mov_b32_dpp v39, v47 row_newbcast:9 row_mask:0xf bank_mask:0xf bound_ctrl:1
	v_mov_b32_dpp v40, v47 row_newbcast:10 row_mask:0xf bank_mask:0xf bound_ctrl:1
	v_mov_b32_dpp v41, v47 row_newbcast:11 row_mask:0xf bank_mask:0xf bound_ctrl:1
	v_mov_b32_dpp v42, v47 row_newbcast:12 row_mask:0xf bank_mask:0xf bound_ctrl:1
	v_mov_b32_dpp v43, v47 row_newbcast:13 row_mask:0xf bank_mask:0xf bound_ctrl:1
	s_waitcnt vmcnt(1)
	v_lshl_add_u32 v72, v80, 9, v87
	v_lshl_add_u32 v73, v81, 9, v87
	v_lshl_add_u32 v74, v82, 9, v87
	global_load_dwordx4 v[50:53], v72, s[24:25]
	global_load_dwordx4 v[46:49], v72, s[24:25] offset:256
	global_load_dwordx4 v[14:17], v73, s[24:25]
	global_load_dwordx4 v[10:13], v73, s[24:25] offset:256
	global_load_dwordx4 v[6:9], v74, s[24:25]
	global_load_dwordx4 v[2:5], v74, s[24:25] offset:256
	v_lshl_add_u32 v75, v84, 8, v54
	v_lshl_add_u32 v78, v84, 7, v88
	v_lshl_add_u32 v76, v85, 8, v54
	v_lshl_add_u32 v79, v85, 7, v88
	v_lshl_add_u32 v77, v86, 8, v54
	v_lshl_add_u32 v80, v86, 7, v88
	global_load_dwordx4 v[30:33], v75, s[26:27]
	global_load_dwordx2 v[70:71], v78, s[28:29]
	global_load_dwordx4 v[26:29], v76, s[26:27]
	global_load_dwordx2 v[66:67], v79, s[28:29]
	global_load_dwordx4 v[18:21], v77, s[26:27]
	global_load_dwordx2 v[68:69], v80, s[28:29]
	s_mov_b32 exec_lo, 0x1ff01ff
	s_mov_b32 exec_hi, 0x1ff01ff
	global_load_dword v120, v144, s[10:11]
	s_mov_b32 exec_lo, 0xe000e00
	s_mov_b32 exec_hi, 0xe000e00
	global_load_dword v120, v145, s[12:13]
	s_mov_b32 exec_lo, 0x70007000
	s_mov_b32 exec_hi, 0x70007000
	global_load_dword v120, v146, s[14:15]
	s_mov_b64 exec, -1
	global_load_dwordx4 v[124:127], v147, s[22:23]
	global_load_dwordx4 v[128:131], v148, s[22:23]
	s_mov_b32 exec_hi, 0
	global_load_dwordx4 v[132:135], v149, s[16:17]
	s_mov_b32 exec_hi, -1
	s_mov_b32 exec_lo, 0
	global_load_dwordx4 v[132:135], v149, s[18:19] offset:-512
	s_mov_b32 exec_lo, -1
	global_load_dwordx4 v[136:139], v150, s[8:9]
	global_load_dwordx4 v[140:143], v150, s[8:9] offset:256
	global_load_dword v119, v150, s[34:35]
	v_mov_b32_e32 v75, 0
	v_mov_b32_e32 v79, 0
	v_mov_b32_e32 v83, 0
	s_waitcnt vmcnt(21)
	v_mfma_f32_16x16x32_fp8_fp8 v[160:163], v[50:51], v[64:65], v[34:37]
	v_mfma_f32_16x16x32_fp8_fp8 v[164:167], v[52:53], v[64:65], v[22:25]
	s_waitcnt vmcnt(20)
	v_mfma_f32_16x16x32_fp8_fp8 v[168:171], v[46:47], v[64:65], v[38:41]
	v_mfma_f32_16x16x32_fp8_fp8 v[172:175], v[48:49], v[64:65], v[42:45]
	s_nop 3
	v_max3_f32 v86, v160, v161, v162
	v_max3_f32 v87, v163, v164, v165
	v_max3_f32 v88, v166, v167, v168
	v_max3_f32 v89, v169, v170, v171
	v_max3_f32 v86, v86, v172, v173
	v_max3_f32 v87, v87, v88, v89
	v_max_f32_e32 v96, v86, v87
	v_mul_f32_e32 v98, 0xbdb8aa3b, v96
	v_pk_fma_f32 v[208:209], v[160:161], s[30:31], v[98:99] op_sel_hi:[1,1,0]
	v_pk_fma_f32 v[210:211], v[162:163], s[30:31], v[98:99] op_sel_hi:[1,1,0]
	v_pk_fma_f32 v[212:213], v[164:165], s[30:31], v[98:99] op_sel_hi:[1,1,0]
	v_pk_fma_f32 v[214:215], v[166:167], s[30:31], v[98:99] op_sel_hi:[1,1,0]
	v_pk_fma_f32 v[216:217], v[168:169], s[30:31], v[98:99] op_sel_hi:[1,1,0]
	v_pk_fma_f32 v[218:219], v[170:171], s[30:31], v[98:99] op_sel_hi:[1,1,0]
	v_pk_fma_f32 v[220:221], v[172:173], s[30:31], v[98:99] op_sel_hi:[1,1,0]
	v_exp_f32_e32 v208, v208
	v_exp_f32_e32 v209, v209
	v_exp_f32_e32 v210, v210
	v_exp_f32_e32 v211, v211
	v_exp_f32_e32 v212, v212
	v_exp_f32_e32 v213, v213
	v_exp_f32_e32 v214, v214
	v_exp_f32_e32 v215, v215
	v_exp_f32_e32 v216, v216
	v_exp_f32_e32 v217, v217
	v_exp_f32_e32 v218, v218
	v_exp_f32_e32 v219, v219
	v_exp_f32_e32 v220, v220
	v_exp_f32_e32 v221, v221
	s_waitcnt vmcnt(19)
	v_mfma_f32_16x16x32_fp8_fp8 v[176:179], v[14:15], v[64:65], v[34:37]
	v_mfma_f32_16x16x32_fp8_fp8 v[180:183], v[16:17], v[64:65], v[22:25]
	s_waitcnt vmcnt(18)
	v_mfma_f32_16x16x32_fp8_fp8 v[184:187], v[10:11], v[64:65], v[38:41]
	v_mfma_f32_16x16x32_fp8_fp8 v[188:191], v[12:13], v[64:65], v[42:45]
	v_pk_add_f32 v[86:87], v[208:209], v[210:211]
	v_pk_add_f32 v[88:89], v[212:213], v[214:215]
	v_pk_add_f32 v[90:91], v[216:217], v[218:219]
	v_pk_mul_f32 v[92:93], v[208:209], v[160:161]
	v_pk_mul_f32 v[94:95], v[210:211], v[162:163]
	v_pk_add_f32 v[86:87], v[86:87], v[220:221]
	v_pk_add_f32 v[88:89], v[88:89], v[90:91]
	v_pk_fma_f32 v[92:93], v[212:213], v[164:165], v[92:93]
	v_pk_fma_f32 v[94:95], v[214:215], v[166:167], v[94:95]
	v_pk_add_f32 v[86:87], v[86:87], v[88:89]
	v_pk_fma_f32 v[92:93], v[216:217], v[168:169], v[92:93]
	v_pk_fma_f32 v[94:95], v[218:219], v[170:171], v[94:95]
	v_add_f32_e32 v86, v86, v87
	v_pk_fma_f32 v[92:93], v[220:221], v[172:173], v[92:93]
	v_rcp_f32_e32 v87, v86
	v_pk_add_f32 v[92:93], v[92:93], v[94:95]
	v_mul_f32_e32 v87, v55, v87
	v_add_f32_e32 v92, v92, v93
	v_mul_f32_e32 v107, v86, v87
	v_mul_f32_e32 v92, v92, v87
	v_mul_f32_e32 v100, 0x43800000, v87
	v_mul_f32_e32 v103, 0x3d800000, v92
	v_max3_f32 v86, v176, v177, v178
	v_max3_f32 v87, v179, v180, v181
	v_max3_f32 v88, v182, v183, v184
	v_max3_f32 v89, v185, v186, v187
	v_max3_f32 v86, v86, v188, v189
	v_max3_f32 v87, v87, v88, v89
	v_max_f32_e32 v96, v86, v87
	v_mul_f32_e32 v98, 0xbdb8aa3b, v96
	v_pk_fma_f32 v[222:223], v[176:177], s[30:31], v[98:99] op_sel_hi:[1,1,0]
	v_pk_fma_f32 v[224:225], v[178:179], s[30:31], v[98:99] op_sel_hi:[1,1,0]
	v_pk_fma_f32 v[226:227], v[180:181], s[30:31], v[98:99] op_sel_hi:[1,1,0]
	v_pk_fma_f32 v[228:229], v[182:183], s[30:31], v[98:99] op_sel_hi:[1,1,0]
	v_pk_fma_f32 v[230:231], v[184:185], s[30:31], v[98:99] op_sel_hi:[1,1,0]
	v_pk_fma_f32 v[232:233], v[186:187], s[30:31], v[98:99] op_sel_hi:[1,1,0]
	v_pk_fma_f32 v[234:235], v[188:189], s[30:31], v[98:99] op_sel_hi:[1,1,0]
	v_exp_f32_e32 v222, v222
	v_exp_f32_e32 v223, v223
	v_exp_f32_e32 v224, v224
	v_exp_f32_e32 v225, v225
	v_exp_f32_e32 v226, v226
	v_exp_f32_e32 v227, v227
	v_exp_f32_e32 v228, v228
	v_exp_f32_e32 v229, v229
	v_exp_f32_e32 v230, v230
	v_exp_f32_e32 v231, v231
	v_exp_f32_e32 v232, v232
	v_exp_f32_e32 v233, v233
	v_exp_f32_e32 v234, v234
	v_exp_f32_e32 v235, v235
	s_waitcnt vmcnt(17)
	v_mfma_f32_16x16x32_fp8_fp8 v[192:195], v[6:7], v[64:65], v[34:37]
	v_mfma_f32_16x16x32_fp8_fp8 v[196:199], v[8:9], v[64:65], v[22:25]
	s_waitcnt vmcnt(16)
	v_mfma_f32_16x16x32_fp8_fp8 v[200:203], v[2:3], v[64:65], v[38:41]
	v_mfma_f32_16x16x32_fp8_fp8 v[204:207], v[4:5], v[64:65], v[42:45]
	v_pk_add_f32 v[86:87], v[222:223], v[224:225]
	v_pk_add_f32 v[88:89], v[226:227], v[228:229]
	v_pk_add_f32 v[90:91], v[230:231], v[232:233]
	v_pk_mul_f32 v[92:93], v[222:223], v[176:177]
	v_pk_mul_f32 v[94:95], v[224:225], v[178:179]
	v_pk_add_f32 v[86:87], v[86:87], v[234:235]
	v_pk_add_f32 v[88:89], v[88:89], v[90:91]
	v_pk_fma_f32 v[92:93], v[226:227], v[180:181], v[92:93]
	v_pk_fma_f32 v[94:95], v[228:229], v[182:183], v[94:95]
	v_pk_add_f32 v[86:87], v[86:87], v[88:89]
	v_pk_fma_f32 v[92:93], v[230:231], v[184:185], v[92:93]
	v_pk_fma_f32 v[94:95], v[232:233], v[186:187], v[94:95]
	v_add_f32_e32 v86, v86, v87
	v_pk_fma_f32 v[92:93], v[234:235], v[188:189], v[92:93]
	v_rcp_f32_e32 v87, v86
	v_pk_add_f32 v[92:93], v[92:93], v[94:95]
	v_mul_f32_e32 v87, v55, v87
	v_add_f32_e32 v92, v92, v93
	v_mul_f32_e32 v108, v86, v87
	v_mul_f32_e32 v92, v92, v87
	v_mul_f32_e32 v101, 0x43800000, v87
	v_mul_f32_e32 v105, 0x3d800000, v92
	v_max3_f32 v86, v192, v193, v194
	v_max3_f32 v87, v195, v196, v197
	v_max3_f32 v88, v198, v199, v200
	v_max3_f32 v89, v201, v202, v203
	v_max3_f32 v86, v86, v204, v205
	v_max3_f32 v87, v87, v88, v89
	v_max_f32_e32 v96, v86, v87
	v_mul_f32_e32 v98, 0xbdb8aa3b, v96
	v_pk_fma_f32 v[236:237], v[192:193], s[30:31], v[98:99] op_sel_hi:[1,1,0]
	v_pk_fma_f32 v[238:239], v[194:195], s[30:31], v[98:99] op_sel_hi:[1,1,0]
	v_pk_fma_f32 v[240:241], v[196:197], s[30:31], v[98:99] op_sel_hi:[1,1,0]
	v_pk_fma_f32 v[242:243], v[198:199], s[30:31], v[98:99] op_sel_hi:[1,1,0]
	v_pk_fma_f32 v[244:245], v[200:201], s[30:31], v[98:99] op_sel_hi:[1,1,0]
	v_pk_fma_f32 v[246:247], v[202:203], s[30:31], v[98:99] op_sel_hi:[1,1,0]
	v_pk_fma_f32 v[248:249], v[204:205], s[30:31], v[98:99] op_sel_hi:[1,1,0]
	v_exp_f32_e32 v236, v236
	v_exp_f32_e32 v237, v237
	v_exp_f32_e32 v238, v238
	v_exp_f32_e32 v239, v239
	v_exp_f32_e32 v240, v240
	v_exp_f32_e32 v241, v241
	v_exp_f32_e32 v242, v242
	v_exp_f32_e32 v243, v243
	v_exp_f32_e32 v244, v244
	v_exp_f32_e32 v245, v245
	v_exp_f32_e32 v246, v246
	v_exp_f32_e32 v247, v247
	v_exp_f32_e32 v248, v248
	v_exp_f32_e32 v249, v249
	v_pk_add_f32 v[86:87], v[236:237], v[238:239]
	v_pk_add_f32 v[88:89], v[240:241], v[242:243]
	v_pk_add_f32 v[90:91], v[244:245], v[246:247]
	v_pk_mul_f32 v[92:93], v[236:237], v[192:193]
	v_pk_mul_f32 v[94:95], v[238:239], v[194:195]
	v_pk_add_f32 v[86:87], v[86:87], v[248:249]
	v_pk_add_f32 v[88:89], v[88:89], v[90:91]
	v_pk_fma_f32 v[92:93], v[240:241], v[196:197], v[92:93]
	v_pk_fma_f32 v[94:95], v[242:243], v[198:199], v[94:95]
	v_pk_add_f32 v[86:87], v[86:87], v[88:89]
	v_pk_fma_f32 v[92:93], v[244:245], v[200:201], v[92:93]
	v_pk_fma_f32 v[94:95], v[246:247], v[202:203], v[94:95]
	v_add_f32_e32 v86, v86, v87
	v_pk_fma_f32 v[92:93], v[248:249], v[204:205], v[92:93]
	v_rcp_f32_e32 v87, v86
	v_pk_add_f32 v[92:93], v[92:93], v[94:95]
	v_mul_f32_e32 v87, v55, v87
	v_add_f32_e32 v92, v92, v93
	v_mul_f32_e32 v109, v86, v87
	v_mul_f32_e32 v92, v92, v87
	v_mul_f32_e32 v102, 0x43800000, v87
	v_mul_f32_e32 v106, 0x3d800000, v92
	v_max3_f32 v122, v103, v105, v106
	v_cmp_gt_u32_e64 s[6:7], 16, v104
	v_mov_b32_e32 v123, v122
	s_nop 1
	v_permlane16_swap_b32_e32 v122, v123
	v_max_f32_e32 v122, v122, v123
	v_mov_b32_e32 v123, v122
	s_nop 1
	v_permlane32_swap_b32_e32 v122, v123
	v_max_f32_e32 v36, v122, v123
	v_mul_f32_e32 v123, 0x3fb8aa3b, v36
	v_fma_f32 v111, v103, v121, -v123
	v_exp_f32_e32 v111, v111
	s_nop 0
	v_mul_f32_e32 v112, v111, v100
	v_mul_f32_e32 v110, v111, v107
	v_mov_b32_e32 v114, v111
	v_pk_mul_f32 v[208:209], v[208:209], v[112:113] op_sel_hi:[1,0]
	v_pk_mul_f32 v[210:211], v[210:211], v[112:113] op_sel_hi:[1,0]
	v_pk_mul_f32 v[212:213], v[212:213], v[112:113] op_sel_hi:[1,0]
	v_pk_mul_f32 v[214:215], v[214:215], v[112:113] op_sel_hi:[1,0]
	v_pk_mul_f32 v[216:217], v[216:217], v[112:113] op_sel_hi:[1,0]
	v_pk_mul_f32 v[218:219], v[218:219], v[112:113] op_sel_hi:[1,0]
	v_pk_mul_f32 v[220:221], v[220:221], v[112:113] op_sel_hi:[1,0]
	s_waitcnt vmcnt(14)
	v_mov_b32_e32 v115, v110
	v_fma_mix_f32 v116, v110, v70, 0 op_sel_hi:[0,1,0]
	v_fma_mix_f32 v117, v110, v70, 0 op_sel:[0,1,0] op_sel_hi:[0,1,0]
	v_fma_mix_f32 v118, v110, v71, 0 op_sel_hi:[0,1,0]
	v_cvt_pk_fp8_f32 v72, v208, v209
	v_cvt_pk_fp8_f32 v73, v212, v213
	v_cvt_pk_fp8_f32 v74, v216, v217
	v_cvt_pk_fp8_f32 v75, v220, v221
	v_cvt_pk_fp8_f32 v72, v210, v211 op_sel:[0,0,1]
	v_cvt_pk_fp8_f32 v73, v214, v215 op_sel:[0,0,1]
	v_cvt_pk_fp8_f32 v74, v218, v219 op_sel:[0,0,1]
	s_nop 1
	v_mfma_f32_16x16x32_fp8_fp8 v[152:155], v[72:73], v[30:31], 0
	v_mfma_f32_16x16x32_fp8_fp8 v[152:155], v[74:75], v[32:33], v[152:155]
	v_fma_f32 v111, v105, v121, -v123
	v_exp_f32_e32 v111, v111
	s_nop 0
	v_mul_f32_e32 v112, v111, v101
	v_mul_f32_e32 v110, v111, v108
	v_add_f32_e32 v114, v114, v111
	v_pk_mul_f32 v[222:223], v[222:223], v[112:113] op_sel_hi:[1,0]
	v_pk_mul_f32 v[224:225], v[224:225], v[112:113] op_sel_hi:[1,0]
	v_pk_mul_f32 v[226:227], v[226:227], v[112:113] op_sel_hi:[1,0]
	v_pk_mul_f32 v[228:229], v[228:229], v[112:113] op_sel_hi:[1,0]
	v_pk_mul_f32 v[230:231], v[230:231], v[112:113] op_sel_hi:[1,0]
	v_pk_mul_f32 v[232:233], v[232:233], v[112:113] op_sel_hi:[1,0]
	v_pk_mul_f32 v[234:235], v[234:235], v[112:113] op_sel_hi:[1,0]
	s_waitcnt vmcnt(12)
	v_add_f32_e32 v115, v115, v110
	v_fma_mix_f32 v116, v110, v66, v116 op_sel_hi:[0,1,0]
	v_fma_mix_f32 v117, v110, v66, v117 op_sel:[0,1,0] op_sel_hi:[0,1,0]
	v_fma_mix_f32 v118, v110, v67, v118 op_sel_hi:[0,1,0]
	v_cvt_pk_fp8_f32 v76, v222, v223
	v_cvt_pk_fp8_f32 v77, v226, v227
	v_cvt_pk_fp8_f32 v78, v230, v231
	v_cvt_pk_fp8_f32 v79, v234, v235
	v_cvt_pk_fp8_f32 v76, v224, v225 op_sel:[0,0,1]
	v_cvt_pk_fp8_f32 v77, v228, v229 op_sel:[0,0,1]
	v_cvt_pk_fp8_f32 v78, v232, v233 op_sel:[0,0,1]
	s_nop 1
	v_mfma_f32_16x16x32_fp8_fp8 v[152:155], v[76:77], v[26:27], v[152:155]
	v_mfma_f32_16x16x32_fp8_fp8 v[152:155], v[78:79], v[28:29], v[152:155]
	v_fma_f32 v111, v106, v121, -v123
	v_exp_f32_e32 v111, v111
	s_nop 0
	v_mul_f32_e32 v112, v111, v102
	v_mul_f32_e32 v110, v111, v109
	v_add_f32_e32 v114, v114, v111
	v_pk_mul_f32 v[236:237], v[236:237], v[112:113] op_sel_hi:[1,0]
	v_pk_mul_f32 v[238:239], v[238:239], v[112:113] op_sel_hi:[1,0]
	v_pk_mul_f32 v[240:241], v[240:241], v[112:113] op_sel_hi:[1,0]
	v_pk_mul_f32 v[242:243], v[242:243], v[112:113] op_sel_hi:[1,0]
	v_pk_mul_f32 v[244:245], v[244:245], v[112:113] op_sel_hi:[1,0]
	v_pk_mul_f32 v[246:247], v[246:247], v[112:113] op_sel_hi:[1,0]
	v_pk_mul_f32 v[248:249], v[248:249], v[112:113] op_sel_hi:[1,0]
	s_waitcnt vmcnt(10)
	v_add_f32_e32 v115, v115, v110
	v_fma_mix_f32 v116, v110, v68, v116 op_sel_hi:[0,1,0]
	v_fma_mix_f32 v117, v110, v68, v117 op_sel:[0,1,0] op_sel_hi:[0,1,0]
	v_fma_mix_f32 v118, v110, v69, v118 op_sel_hi:[0,1,0]
	v_cvt_pk_fp8_f32 v80, v236, v237
	v_cvt_pk_fp8_f32 v81, v240, v241
	v_cvt_pk_fp8_f32 v82, v244, v245
	v_cvt_pk_fp8_f32 v83, v248, v249
	v_cvt_pk_fp8_f32 v80, v238, v239 op_sel:[0,0,1]
	v_cvt_pk_fp8_f32 v81, v242, v243 op_sel:[0,0,1]
	v_cvt_pk_fp8_f32 v82, v246, v247 op_sel:[0,0,1]
	s_nop 1
	v_mfma_f32_16x16x32_fp8_fp8 v[152:155], v[80:81], v[18:19], v[152:155]
	v_mfma_f32_16x16x32_fp8_fp8 v[152:155], v[82:83], v[20:21], v[152:155]
	v_mov_b32_e32 v86, v114
	v_mov_b32_e32 v87, v115
	v_mov_b32_e32 v88, v116
	v_mov_b32_e32 v89, v117
	v_mov_b32_e32 v90, v118
	v_permlane16_swap_b32_e32 v114, v86
	v_permlane16_swap_b32_e32 v115, v87
	v_permlane16_swap_b32_e32 v116, v88
	v_permlane16_swap_b32_e32 v117, v89
	v_permlane16_swap_b32_e32 v118, v90
	v_add_f32_e32 v114, v114, v86
	v_add_f32_e32 v115, v115, v87
	v_add_f32_e32 v116, v116, v88
	v_add_f32_e32 v117, v117, v89
	v_add_f32_e32 v118, v118, v90
	v_mov_b32_e32 v86, v114
	v_mov_b32_e32 v87, v115
	v_mov_b32_e32 v88, v116
	v_mov_b32_e32 v89, v117
	v_mov_b32_e32 v90, v118
	v_permlane32_swap_b32_e32 v114, v86
	v_permlane32_swap_b32_e32 v115, v87
	v_permlane32_swap_b32_e32 v116, v88
	v_permlane32_swap_b32_e32 v117, v89
	v_permlane32_swap_b32_e32 v118, v90
	v_add_f32_e32 v37, v114, v86
	v_add_f32_e32 v20, v115, v87
	v_add_f32_e32 v18, v116, v88
	v_add_f32_e32 v19, v117, v89
	v_add_f32_e32 v21, v118, v90
	ds_write2_b32 v156, v152, v153 offset0:0 offset1:20
	ds_write2_b32 v156, v154, v155 offset0:40 offset1:60
	s_branch .LBB1_30
.LBB1_16:
	s_mov_b32 exec_lo, 0x1ff01ff
	s_mov_b32 exec_hi, 0x1ff01ff
	global_load_dword v120, v144, s[10:11]
	s_mov_b32 exec_lo, 0xe000e00
	s_mov_b32 exec_hi, 0xe000e00
	global_load_dword v120, v145, s[12:13]
	s_mov_b32 exec_lo, 0x70007000
	s_mov_b32 exec_hi, 0x70007000
	global_load_dword v120, v146, s[14:15]
	s_mov_b64 exec, -1
	global_load_dwordx4 v[124:127], v147, s[22:23]
	global_load_dwordx4 v[128:131], v148, s[22:23]
	s_mov_b32 exec_hi, 0
	global_load_dwordx4 v[132:135], v149, s[16:17]
	s_mov_b32 exec_hi, -1
	s_mov_b32 exec_lo, 0
	global_load_dwordx4 v[132:135], v149, s[18:19] offset:-512
	s_mov_b32 exec_lo, -1
	global_load_dwordx4 v[136:139], v150, s[8:9]
	global_load_dwordx4 v[140:143], v150, s[8:9] offset:256
	global_load_dword v119, v150, s[34:35]
	v_mov_b32_e32 v21, 0
	ds_write2_b32 v156, v21, v21 offset1:20
	ds_write2_b32 v156, v21, v21 offset0:40 offset1:60
	v_cmp_gt_u32_e64 s[6:7], 16, v104
	v_mov_b32_e32 v37, 1.0
	v_mov_b32_e32 v20, 0
	v_mov_b32_e32 v19, 0
	v_mov_b32_e32 v18, 0
	v_mov_b32_e32 v36, 0

.LBB1_32:
	s_or_b64 exec, exec, s[8:9]
	s_movk_i32 s6, 0x100
	v_cmp_gt_u32_e64 s[6:7], s6, v0
	s_waitcnt lgkmcnt(0)
	s_barrier
	s_and_saveexec_b64 s[14:15], s[6:7]
	s_cbranch_execz .LBB1_39
	ds_read_b96 v[160:162], v157 offset:12288
	ds_read_b96 v[164:166], v157 offset:12800
	ds_read_b96 v[168:170], v157 offset:13312
	ds_read_b96 v[172:174], v157 offset:13824
	ds_read2st64_b32 v[176:177], v158 offset0:48 offset1:50
	ds_read2st64_b32 v[178:179], v158 offset0:52 offset1:54
	ds_read2st64_b32 v[180:181], v159 offset0:28 offset1:33
	ds_read2st64_b32 v[182:183], v159 offset0:38 offset1:43
	v_cmp_gt_u32_e32 vcc, 3, v57
	v_cndmask_b32_e64 v18, 1.0, 0, s[20:21]
	s_waitcnt lgkmcnt(4)
	v_max_f32_e32 v21, v160, v164
	v_max3_f32 v33, v21, v168, v172
	v_sub_f32_e32 v21, v160, v33
	v_sub_f32_e32 v29, v164, v33
	v_sub_f32_e32 v30, v168, v33
	v_sub_f32_e32 v33, v172, v33
	v_mul_f32_e32 v21, 0x3fb8aa3b, v21
	v_mul_f32_e32 v29, 0x3fb8aa3b, v29
	v_mul_f32_e32 v30, 0x3fb8aa3b, v30
	v_mul_f32_e32 v33, 0x3fb8aa3b, v33
	v_exp_f32_e32 v21, v21
	v_exp_f32_e32 v29, v29
	v_exp_f32_e32 v30, v30
	v_exp_f32_e32 v33, v33
	v_mov_b32_e32 v20, v250
	v_mul_f32_e32 v35, v21, v161
	v_mul_f32_e32 v34, v21, v162
	v_fmac_f32_e32 v35, v29, v165
	v_fmac_f32_e32 v34, v29, v166
	v_fmac_f32_e32 v35, v30, v169
	v_fmac_f32_e32 v34, v30, v170
	v_fmac_f32_e32 v35, v33, v173
	v_fmac_f32_e32 v34, v33, v174
	v_rcp_f32_e32 v35, v35
	s_waitcnt lgkmcnt(0)
	v_mul_f32_e32 v31, v21, v180
	v_mul_f32_e32 v18, v18, v35
	v_fmac_f32_e32 v31, v29, v181
	v_mul_f32_e32 v35, v21, v176
	v_fmac_f32_e32 v31, v30, v182
	v_fmac_f32_e32 v35, v29, v177
	v_fmac_f32_e32 v31, v33, v183
	v_fmac_f32_e32 v35, v30, v178
	v_mul_f32_e32 v31, v31, v18
	v_fmac_f32_e32 v35, v33, v179
	s_mov_b32 s8, 0x3a800000
	v_fma_mixlo_f16 v31, v31, s8, 0
	v_cmp_eq_u32_e64 s[8:9], 7, v57
	s_and_saveexec_b64 s[10:11], s[4:5]
	ds_write_b16 v251, v31
	s_and_b64 exec, exec, s[8:9]
	v_mov_b32_e32 v31, 0x3c00
	ds_write_b16 v20, v31 offset:46
	s_or_b64 exec, exec, s[10:11]
	s_waitcnt vmcnt(7)
	v_mov_b32_dpp v33, v120 row_newbcast:10 row_mask:0xf bank_mask:0xf bound_ctrl:1
	v_mov_b32_dpp v36, v120 row_newbcast:11 row_mask:0xf bank_mask:0xf bound_ctrl:1
	v_cmp_eq_u32_e64 s[10:11], 1, v57
	v_mov_b32_dpp v32, v120 row_newbcast:9 row_mask:0xf bank_mask:0xf bound_ctrl:1
	v_mov_b32_dpp v38, v120 row_newbcast:13 row_mask:0xf bank_mask:0xf bound_ctrl:1
	v_mov_b32_dpp v39, v120 row_newbcast:14 row_mask:0xf bank_mask:0xf bound_ctrl:1
	v_cndmask_b32_e64 v33, v36, v33, s[10:11]
	v_cmp_eq_u32_e64 s[8:9], 0, v57
	v_mov_b32_dpp v37, v120 row_newbcast:12 row_mask:0xf bank_mask:0xf bound_ctrl:1
	v_mov_b32_dpp v27, v120 row_newbcast:0 row_mask:0xf bank_mask:0xf bound_ctrl:1
	v_cndmask_b32_e64 v32, v33, v32, s[8:9]
	v_cndmask_b32_e64 v33, v39, v38, s[10:11]
	v_cndmask_b32_e64 v33, v33, v37, s[8:9]
	v_fma_f32 v33, v34, v33, -v35
	v_fma_f32 v32, v18, v33, -v32
	v_mov_b32_dpp v20, v120 row_newbcast:1 row_mask:0xf bank_mask:0xf bound_ctrl:1
	v_mov_b32_dpp v19, v120 row_newbcast:2 row_mask:0xf bank_mask:0xf bound_ctrl:1
	v_mov_b32_dpp v31, v120 row_newbcast:3 row_mask:0xf bank_mask:0xf bound_ctrl:1
	v_mov_b32_dpp v29, v120 row_newbcast:4 row_mask:0xf bank_mask:0xf bound_ctrl:1
	v_mov_b32_dpp v26, v120 row_newbcast:5 row_mask:0xf bank_mask:0xf bound_ctrl:1
	v_mov_b32_dpp v30, v120 row_newbcast:6 row_mask:0xf bank_mask:0xf bound_ctrl:1
	v_mov_b32_dpp v28, v120 row_newbcast:7 row_mask:0xf bank_mask:0xf bound_ctrl:1
	v_mov_b32_dpp v21, v120 row_newbcast:8 row_mask:0xf bank_mask:0xf bound_ctrl:1
	v_mov_b32_dpp v18, v32 quad_perm:[0,0,0,0] row_mask:0xf bank_mask:0xf bound_ctrl:1
	v_mov_b32_dpp v33, v32 quad_perm:[1,1,1,1] row_mask:0xf bank_mask:0xf bound_ctrl:1
	v_mov_b32_dpp v32, v32 quad_perm:[2,2,2,2] row_mask:0xf bank_mask:0xf bound_ctrl:1
	s_and_b64 s[12:13], vcc, s[4:5]
	s_and_b64 exec, exec, s[12:13]
	s_cbranch_execz .LBB1_39
	v_mul_f32_e32 v31, v31, v33
	v_fmac_f32_e32 v31, v27, v18
	v_mul_f32_e32 v27, v29, v33
	v_fmac_f32_e32 v27, v20, v18
	v_fmac_f32_e32 v27, v28, v32
	v_mul_f32_e32 v20, v26, v33
	v_fmac_f32_e32 v31, v30, v32
	v_fmac_f32_e32 v20, v19, v18
	v_mul_f32_e32 v18, v27, v27
	v_fmac_f32_e32 v20, v21, v32
	v_fmac_f32_e32 v18, v31, v31
	v_fmac_f32_e32 v18, v20, v20
	v_mad_u32_u24 v26, v56, 3, v57
	v_sqrt_f32_e32 v18, v18
	v_cndmask_b32_e64 v19, v20, v27, s[10:11]
	v_add_u32_e32 v29, 56, v26
	v_add_f32_e32 v21, 0x38d1b717, v18
	v_rcp_f32_e32 v21, v21
	v_cndmask_b32_e64 v20, v19, v31, s[8:9]
	v_mul_u32_u24_e32 v28, 0x2493, v26
	v_mul_u32_u24_e32 v30, 0x2493, v29
	v_lshrrev_b32_e32 v28, 16, v28
	v_lshrrev_b32_e32 v30, 16, v30
	v_mul_u32_u24_e32 v28, 66, v28
	v_mul_u32_u24_e32 v30, 66, v30
	v_lshl_add_u32 v28, v26, 1, v28
	v_lshl_add_u32 v30, v29, 1, v30
	v_cvt_f16_f32_e32 v27, v20
	v_fma_mixlo_f16 v20, v20, v21, 0
	ds_write_b16 v28, v27 offset:14368
	ds_write_b16 v30, v20 offset:14368
	s_and_b64 exec, exec, s[8:9]
	s_cbranch_execz .LBB1_39
	v_cmp_lt_u32_e32 vcc, 6, v56
	v_cvt_f16_f32_e32 v18, v18
	v_lshlrev_b32_e32 v19, 1, v56
	v_mov_b32_e32 v20, 0x42
	v_cndmask_b32_e32 v20, 0, v20, vcc
	v_add_u32_e32 v19, v19, v20
	ds_write_b16 v19, v18 offset:14848
.LBB1_39:
	s_or_b64 exec, exec, s[14:15]
	s_load_dwordx2 s[14:15], s[0:1], 0x38
	v_cmp_eq_u32_e32 vcc, 3, v63
	s_and_saveexec_b64 s[0:1], vcc
	s_cbranch_execz .LBB1_41
	v_lshlrev_b32_e32 v18, 4, v104
	s_waitcnt vmcnt(3)
	ds_write_b128 v18, v[132:135] offset:15616
.LBB1_41:
	s_or_b64 exec, exec, s[0:1]
	v_bfe_u32 v41, s3, v56, 1
	v_mov_b32_e32 v40, v254
	v_cvt_f32_u32_e32 v41, v41
	s_waitcnt lgkmcnt(0)
	s_barrier
	ds_read_b128 v[18:21], v252 offset:14336
	s_waitcnt vmcnt(5) lgkmcnt(0)
	v_mfma_f32_16x16x32_f16 v[14:17], v[18:21], v[124:127], 0
	v_mfma_f32_16x16x32_f16 v[6:9], v[18:21], v[128:131], 0
	s_nop 6
	ds_write2st64_b32 v253, v14, v15 offset1:2
	ds_write2st64_b32 v253, v16, v17 offset0:4 offset1:6
	ds_write2st64_b32 v253, v6, v7 offset0:1 offset1:3
	ds_write2st64_b32 v253, v8, v9 offset0:5 offset1:7
	s_waitcnt lgkmcnt(0)
	s_barrier
	s_and_saveexec_b64 s[0:1], s[4:5]
	s_cbranch_execz .LBB1_53
	ds_read_b128 v[14:17], v255
	ds_read_b128 v[6:9], v255 offset:256
	ds_read_b128 v[24:27], v54 offset:15616
	ds_read_b128 v[28:31], v54 offset:15872
	ds_read_b128 v[32:35], v54 offset:16128
	ds_read_b128 v[36:39], v54 offset:16384
	s_waitcnt vmcnt(1) lgkmcnt(4)
	v_pk_fma_f32 v[136:137], v[14:15], v[40:41], v[136:137] op_sel:[0,1,0]
	v_pk_fma_f32 v[138:139], v[16:17], v[40:41], v[138:139] op_sel:[0,1,0]
	v_pk_fma_f32 v[140:141], v[6:7], v[40:41], v[140:141] op_sel:[0,1,0]
	v_pk_fma_f32 v[142:143], v[8:9], v[40:41], v[142:143] op_sel:[0,1,0]
	v_pk_add_f32 v[10:11], v[136:137], v[138:139]
	v_pk_add_f32 v[12:13], v[140:141], v[142:143]
	v_mov_b32_e32 v15, 0x3727c5ac
	v_pk_add_f32 v[10:11], v[10:11], v[12:13]
	s_nop 0
	v_add_f32_e32 v10, v10, v11
	s_nop 1
	v_add_f32_dpp v10, v10, v10 quad_perm:[1,0,3,2] row_mask:0xf bank_mask:0xf bound_ctrl:1
	s_nop 1
	v_add_f32_dpp v10, v10, v10 quad_perm:[2,3,0,1] row_mask:0xf bank_mask:0xf bound_ctrl:1
	s_nop 1
	v_add_f32_dpp v10, v10, v10 row_half_mirror row_mask:0xf bank_mask:0xf bound_ctrl:1
	s_nop 1
	v_add_f32_dpp v10, v10, v10 row_mirror row_mask:0xf bank_mask:0xf bound_ctrl:1
	v_mul_f32_e32 v10, 0x3c000000, v10
	v_pk_add_f32 v[136:137], v[136:137], v[10:11] op_sel_hi:[1,0] neg_lo:[0,1] neg_hi:[0,1]
	v_pk_add_f32 v[138:139], v[138:139], v[10:11] op_sel_hi:[1,0] neg_lo:[0,1] neg_hi:[0,1]
	v_pk_add_f32 v[140:141], v[140:141], v[10:11] op_sel_hi:[1,0] neg_lo:[0,1] neg_hi:[0,1]
	v_pk_add_f32 v[142:143], v[142:143], v[10:11] op_sel_hi:[1,0] neg_lo:[0,1] neg_hi:[0,1]
	v_pk_mul_f32 v[12:13], v[136:137], v[136:137]
	v_pk_mul_f32 v[16:17], v[138:139], v[138:139]
	v_pk_fma_f32 v[12:13], v[140:141], v[140:141], v[12:13]
	v_pk_fma_f32 v[16:17], v[142:143], v[142:143], v[16:17]
	s_nop 0
	v_pk_add_f32 v[12:13], v[12:13], v[16:17]
	s_nop 0
	v_add_f32_e32 v12, v12, v13
	s_nop 1
	v_add_f32_dpp v12, v12, v12 quad_perm:[1,0,3,2] row_mask:0xf bank_mask:0xf bound_ctrl:1
	s_nop 1
	v_add_f32_dpp v12, v12, v12 quad_perm:[2,3,0,1] row_mask:0xf bank_mask:0xf bound_ctrl:1
	s_nop 1
	v_add_f32_dpp v12, v12, v12 row_half_mirror row_mask:0xf bank_mask:0xf bound_ctrl:1
	s_nop 1
	v_add_f32_dpp v12, v12, v12 row_mirror row_mask:0xf bank_mask:0xf bound_ctrl:1
	v_fmac_f32_e32 v15, 0x3c000000, v12
	v_rsq_f32_e32 v14, v15
	s_nop 0
	v_pk_mul_f32 v[136:137], v[136:137], v[14:15] op_sel_hi:[1,0]
	v_pk_mul_f32 v[138:139], v[138:139], v[14:15] op_sel_hi:[1,0]
	v_pk_mul_f32 v[140:141], v[140:141], v[14:15] op_sel_hi:[1,0]
	v_pk_mul_f32 v[142:143], v[142:143], v[14:15] op_sel_hi:[1,0]
	s_waitcnt lgkmcnt(0)
	v_pk_fma_f32 v[136:137], v[24:25], v[136:137], v[32:33]
	v_pk_fma_f32 v[138:139], v[26:27], v[138:139], v[34:35]
	v_pk_fma_f32 v[140:141], v[28:29], v[140:141], v[36:37]
	v_pk_fma_f32 v[142:143], v[30:31], v[142:143], v[38:39]
	global_store_dwordx4 v40, v[136:139], s[14:15] nt
	global_store_dwordx4 v40, v[140:143], s[14:15] offset:256 nt

	.amdhsa_kernel _Z11attn_kernelILi4EEvPKfS1_S1_S1_S1_S1_PKcPf
		.amdhsa_group_segment_fixed_size 16640
		.amdhsa_private_segment_fixed_size 0
		.amdhsa_kernarg_size 64
		.amdhsa_user_sgpr_count 2
		.amdhsa_user_sgpr_dispatch_ptr 0
		.amdhsa_user_sgpr_queue_ptr 0
		.amdhsa_user_sgpr_kernarg_segment_ptr 1
		.amdhsa_user_sgpr_dispatch_id 0
		.amdhsa_user_sgpr_kernarg_preload_length 0
		.amdhsa_user_sgpr_kernarg_preload_offset 0
		.amdhsa_user_sgpr_private_segment_size 0
		.amdhsa_uses_dynamic_stack 0
		.amdhsa_enable_private_segment 0
		.amdhsa_system_sgpr_workgroup_id_x 1
		.amdhsa_system_sgpr_workgroup_id_y 0
		.amdhsa_system_sgpr_workgroup_id_z 0
		.amdhsa_system_sgpr_workgroup_info 0
		.amdhsa_system_vgpr_workitem_id 0
		.amdhsa_next_free_vgpr 256
		.amdhsa_next_free_sgpr 36
		.amdhsa_accum_offset 256
		.amdhsa_reserve_vcc 1
		.amdhsa_float_round_mode_32 0
		.amdhsa_float_round_mode_16_64 0
		.amdhsa_float_denorm_mode_32 3
		.amdhsa_float_denorm_mode_16_64 3
		.amdhsa_dx10_clamp 1
		.amdhsa_ieee_mode 1
		.amdhsa_fp16_overflow 0
		.amdhsa_tg_split 0
		.amdhsa_exception_fp_ieee_invalid_op 0
		.amdhsa_exception_fp_denorm_src 0
		.amdhsa_exception_fp_ieee_div_zero 0
		.amdhsa_exception_fp_ieee_overflow 0
		.amdhsa_exception_fp_ieee_underflow 0
		.amdhsa_exception_fp_ieee_inexact 0
		.amdhsa_exception_int_div_zero 0
	.end_amdhsa_kernel

amdhsa.kernels:
  - .agpr_count:     0
    .args:
      - .actual_access:  read_only
        .address_space:  global
        .offset:         0
        .size:           8
        .value_kind:     global_buffer
      - .actual_access:  read_only
        .address_space:  global
        .offset:         8
        .size:           8
        .value_kind:     global_buffer
      - .actual_access:  read_only
        .address_space:  global
        .offset:         16
        .size:           8
        .value_kind:     global_buffer
      - .actual_access:  read_only
        .address_space:  global
        .offset:         24
        .size:           8
        .value_kind:     global_buffer
      - .actual_access:  read_only
        .address_space:  global
        .offset:         32
        .size:           8
        .value_kind:     global_buffer
      - .actual_access:  read_only
        .address_space:  global
        .offset:         40
        .size:           8
        .value_kind:     global_buffer
      - .actual_access:  read_only
        .address_space:  global
        .offset:         48
        .size:           8
        .value_kind:     global_buffer
      - .actual_access:  read_only
        .address_space:  global
        .offset:         56
        .size:           8
        .value_kind:     global_buffer
      - .actual_access:  read_only
        .address_space:  global
        .offset:         64
        .size:           8
        .value_kind:     global_buffer
      - .actual_access:  read_only
        .address_space:  global
        .offset:         72
        .size:           8
        .value_kind:     global_buffer
      - .actual_access:  write_only
        .address_space:  global
        .offset:         80
        .size:           8
        .value_kind:     global_buffer
    .group_segment_fixed_size: 13056
    .kernarg_segment_align: 8
    .kernarg_segment_size: 88
    .language:       OpenCL C
    .language_version:
      - 2
      - 0
    .max_flat_workgroup_size: 128
    .name:           _Z11prep_kernelPKfS0_PKiS2_S0_S0_S0_S0_S0_S0_Pc
    .private_segment_fixed_size: 0
    .sgpr_count:     41
    .sgpr_spill_count: 0
    .symbol:         _Z11prep_kernelPKfS0_PKiS2_S0_S0_S0_S0_S0_S0_Pc.kd
    .uniform_work_group_size: 1
    .uses_dynamic_stack: false
    .vgpr_count:     200
    .vgpr_spill_count: 0
    .wavefront_size: 64
  - .agpr_count:     0
    .args:
      - .actual_access:  read_only
        .address_space:  global
        .offset:         0
        .size:           8
        .value_kind:     global_buffer
      - .actual_access:  read_only
        .address_space:  global
        .offset:         8
        .size:           8
        .value_kind:     global_buffer
      - .actual_access:  read_only
        .address_space:  global
        .offset:         16
        .size:           8
        .value_kind:     global_buffer
      - .actual_access:  read_only
        .address_space:  global
        .offset:         24
        .size:           8
        .value_kind:     global_buffer
      - .actual_access:  read_only
        .address_space:  global
        .offset:         32
        .size:           8
        .value_kind:     global_buffer
      - .actual_access:  read_only
        .address_space:  global
        .offset:         40
        .size:           8
        .value_kind:     global_buffer
      - .actual_access:  read_only
        .address_space:  global
        .offset:         48
        .size:           8
        .value_kind:     global_buffer
      - .actual_access:  write_only
        .address_space:  global
        .offset:         56
        .size:           8
        .value_kind:     global_buffer
    .group_segment_fixed_size: 16640
    .kernarg_segment_align: 8
    .kernarg_segment_size: 64
    .language:       OpenCL C
    .language_version:
      - 2
      - 0
    .max_flat_workgroup_size: 256
    .name:           _Z11attn_kernelILi4EEvPKfS1_S1_S1_S1_S1_PKcPf
    .private_segment_fixed_size: 0
    .sgpr_count:     42
    .sgpr_spill_count: 0
    .symbol:         _Z11attn_kernelILi4EEvPKfS1_S1_S1_S1_S1_PKcPf.kd
    .uniform_work_group_size: 1
    .uses_dynamic_stack: false
    .vgpr_count:     256
    .vgpr_spill_count: 0
    .wavefront_size: 64
